# grid barrier: follower workgroups invalidate only their L1 (buffer_inv sc0); the XCD-last workgroup's buffer_inv sc1 already invalidated the XCD L2 before releasing them (relay protocol as baseline)
# speedup vs baseline: 1.0229x; 1.0229x over previous
.LBB0_220:
	s_or_b64 exec, exec, s[10:11]
	s_waitcnt vmcnt(0)
	buffer_inv sc0
	s_waitcnt vmcnt(0)

.LBB0_308:
	s_or_b64 exec, exec, s[8:9]
	s_waitcnt vmcnt(0)
	buffer_inv sc0
	s_waitcnt vmcnt(0)
